# prep phase: upper-half workgroups run the compute-bound Fourier-weight fold (WcsT) first and the HBM-streaming parts after, overlapping the co-resident lower-half workgroups' streaming
# speedup vs baseline: 1.0060x; 1.0060x over previous
; __device__ void phase_prep(KParams& p, int bid, int nb, char* smem) {
;   float* sm = reinterpret_cast<float*>(smem);
;   const int tid = threadIdx.x;
;   if (bid == 0 && tid < 64) p.ctr[tid] = 0u;
;   {
;     float* t256 = reinterpret_cast<float*>(smem + 20480);
;     float* t2048 = reinterpret_cast<float*>(smem + 24576);
;     t256[tid] = cospif((float)tid * (1.0f / 128.f));
;     for (int i = tid; i < 2048; i += NTHREADS) t2048[i] = cospif((float)i * (1.0f / 1024.f));
;     __syncthreads();
;   }
;   for (int t = bid; t < 48 * KSPLIT; t += nb) adaln_partial_task(p, t, sm);
.LBB0_13:
	s_or_b64 exec, exec, s[16:17]
	v_and_b32_e32 v184, 63, v0
	s_waitcnt lgkmcnt(0)
	s_barrier
	s_mov_b32 s99, 0
	s_cmpk_lt_u32 s2, 0x100
	s_cbranch_scc1 .Lmy_A
	s_cmpk_lg_u32 s34, 0x200
	s_cbranch_scc1 .Lmy_A
	s_mov_b32 s99, 1
	s_branch .Lmy_E
.Lmy_A:
	s_cmpk_gt_i32 s2, 0x5ff
	s_cbranch_scc1 .LBB0_19
	s_load_dwordx2 s[14:15], s[12:13], 0x8
	s_load_dwordx4 s[8:11], s[12:13], 0x18
	s_load_dwordx2 s[16:17], s[12:13], 0x180
	s_movk_i32 s3, 0x140
	v_cmp_gt_u32_e64 s[6:7], s3, v0
	v_lshlrev_b32_e32 v1, 5, v0
	s_movk_i32 s3, 0x100
	s_mov_b32 s22, 0xc000
	s_mov_b32 s23, 0x18000
	s_mov_b32 s24, 0x24000
	s_mov_b32 s25, 0x30000
	s_mov_b32 s26, 0x3c000
	s_mov_b32 s27, 0x48000
	s_mov_b32 s28, 0x54000
	s_mov_b32 s29, 0x60000
	s_mov_b32 s30, 0x6c000
	s_mov_b32 s31, 0x78000
	s_mov_b32 s35, 0x84000
	s_mov_b32 s36, 0x90000
	s_mov_b32 s37, 0x9c000
	s_mov_b32 s38, 0xa8000
	s_mov_b32 s39, 0xb4000
	s_mov_b32 s40, 0xc0000
	s_mov_b32 s41, 0xcc000
	s_mov_b32 s42, 0xd8000
	s_mov_b32 s43, 0xe4000
	s_mov_b32 s46, 0xf0000
	s_mov_b32 s47, 0xfc000
	s_mov_b32 s48, 0x108000
	s_mov_b32 s49, 0x114000
	s_mov_b32 s50, 0x120000
	s_mov_b32 s51, 0x12c000
	s_mov_b32 s52, 0x138000
	s_mov_b32 s53, 0x144000
	s_mov_b32 s54, 0x150000
	s_mov_b32 s55, 0x15c000
	s_mov_b32 s56, 0x168000
	s_mov_b32 s57, 0x174000
	s_mov_b32 s58, 0x180000
	s_mov_b32 s59, 0x18c000
	s_mov_b32 s60, 0x198000
	s_mov_b32 s61, 0x1a4000
	s_mov_b32 s62, 0x1b0000
	s_mov_b32 s63, 0x1bc000
	s_mov_b32 s64, 0x1c8000
	s_mov_b32 s65, 0x1d4000
	s_mov_b32 s66, 0x1e0000
	s_mov_b32 s67, 0x1ec000
	s_mov_b32 s68, 0x1f8000
	s_mov_b32 s69, 0x204000
	s_mov_b32 s70, 0x210000
	s_mov_b32 s71, 0x21c000
	s_mov_b32 s72, 0x228000
	s_mov_b32 s73, 0x234000
	s_mov_b32 s74, 0x240000
	s_mov_b32 s75, 0x24c000
	s_mov_b32 s76, 0x258000
	s_mov_b32 s77, 0x264000
	s_mov_b32 s78, 0x270000
	s_mov_b32 s79, 0x27c000
	s_mov_b32 s80, 0x288000
	s_mov_b32 s81, 0x294000
	s_mov_b32 s82, 0x2a0000
	s_mov_b32 s83, 0x2ac000
	s_mov_b32 s84, 0x2b8000
	s_mov_b32 s85, 0x2c4000
	s_mov_b32 s86, 0x2d0000
	s_mov_b32 s87, 0x2dc000
	s_mov_b32 s88, 0x2e8000
	s_mov_b32 s89, 0x2f4000
	v_mov_b32_e32 v6, 0
	s_mov_b32 s90, s2
	s_branch .LBB0_16

; __device__ void phase_prep(KParams& p, int bid, int nb, char* smem) {
;     ...
;   {
;     const float* t256 = reinterpret_cast<const float*>(smem + 20480);
;     const float scale = 1.0f / sqrtf((float)L * 256.f);
;     const int vb = (bid + (nb >> 1)) % nb;
;     for (int i = vb * NTHREADS + tid; i < 4 * 64 * 256; i += nb * NTHREADS) {
;       const int d = i & 255, cg = (i >> 8) & 63, g = i >> 14;
;       float c0_ = 0.f, c1_ = 0.f, c2_ = 0.f, c3_ = 0.f, s0_ = 0.f, s1_ = 0.f, s2_ = 0.f, s3_ = 0.f;
;       const float* wp = p.w_fmix + (size_t)g * 65536 + d;
; #pragma unroll 1
.LBB0_48:
	s_or_b64 exec, exec, s[14:15]
	s_cmp_eq_u32 s99, 2
	s_cbranch_scc1 .Lmy_F
.Lmy_E:
	s_abs_i32 s3, s34
	v_cvt_f32_u32_e32 v1, s3
	s_sub_i32 s7, 0, s3
	s_ashr_i32 s6, s34, 1
	s_add_i32 s6, s6, s2
	v_rcp_iflag_f32_e32 v1, v1
	s_ashr_i32 s8, s6, 31
	s_abs_i32 s6, s6
	v_mul_f32_e32 v1, 0x4f7ffffe, v1
	v_cvt_u32_f32_e32 v1, v1
	s_nop 0
	v_readfirstlane_b32 s9, v1
	s_mul_i32 s7, s7, s9
	s_mul_hi_u32 s7, s9, s7
	s_add_i32 s9, s9, s7
	s_mul_hi_u32 s7, s6, s9
	s_mul_i32 s7, s7, s3
	s_sub_i32 s6, s6, s7
	s_sub_i32 s7, s6, s3
	s_cmp_ge_u32 s6, s3
	s_cselect_b32 s6, s7, s6
	s_sub_i32 s7, s6, s3
	s_cmp_ge_u32 s6, s3
	s_cselect_b32 s3, s7, s6
	s_xor_b32 s3, s3, s8
	s_sub_i32 s3, s3, s8
	v_lshl_or_b32 v1, s3, 8, v0
	s_mov_b32 s3, 0x10000
	v_cmp_gt_i32_e32 vcc, s3, v1
	s_and_saveexec_b64 s[6:7], vcc
	s_cbranch_execz .LBB0_53
	s_load_dwordx2 s[8:9], s[12:13], 0x168
	s_load_dwordx2 s[10:11], s[12:13], 0x58
	v_mov_b32_e32 v3, 0
	v_lshlrev_b32_e32 v2, 9, v0
	v_mov_b32_e32 v183, v3
	s_waitcnt lgkmcnt(0)
	v_lshl_add_u64 v[4:5], s[8:9], 0, v[2:3]
	v_lshl_add_u64 v[8:9], s[10:11], 0, v[182:183]
	s_mov_b64 s[8:9], 0x3c00
	s_lshl_b32 s3, s34, 8
	v_lshl_add_u64 v[8:9], v[8:9], 0, s[8:9]
	s_mov_b64 s[8:9], 0
	s_movk_i32 s15, 0xd000
	s_movk_i32 s16, 0xe000
	s_movk_i32 s17, 0xf000
	s_mov_b64 s[10:11], 0x4000
	s_mov_b32 s14, 0x3ab504f3
	s_mov_b32 s18, 0xffff
	v_mov_b32_e32 v23, 2

; __device__ void phase_prep(KParams& p, int bid, int nb, char* smem) {
;     ...
;   {
;     const float* t2048 = reinterpret_cast<const float*>(smem + 24576);
;     for (size_t i = (size_t)bid * NTHREADS + tid; i < (size_t)1024 * 2048 / 8; i += (size_t)nb * NTHREADS) {
;       const int k = (int)(i / 256), j = (int)(i % 256) * 8;
;       const bool iss = j >= 1024;
.LBB0_53:
	s_or_b64 exec, exec, s[6:7]
	s_cmp_eq_u32 s99, 1
	s_cbranch_scc0 .Lmy_F
	s_mov_b32 s99, 2
	s_branch .Lmy_A
.Lmy_F:
	s_mov_b64 s[6:7], 0x40000
	v_cmp_gt_u64_e32 vcc, s[6:7], v[6:7]
	s_and_saveexec_b64 s[6:7], vcc
	s_cbranch_execz .LBB0_56
	s_load_dwordx2 s[8:9], s[12:13], 0x170
	s_ashr_i32 s35, s34, 31
	v_lshlrev_b32_e32 v1, 3, v0
	s_lshl_b64 s[10:11], s[34:35], 8
	v_lshl_or_b32 v1, s2, 11, v1
	s_lshl_b32 s3, s34, 11
	s_mov_b64 s[12:13], 0
	s_movk_i32 s16, 0x3ff
	v_mov_b32_e32 v3, 0
	s_mov_b64 s[14:15], 0x3ffff
